# baseline (speedup 1.0000x reference)
_Z6scan_kPKDF16_S0_S0_S0_PKfPf:
	s_load_dwordx8 s[4:11], s[0:1], 0x0
	s_load_dwordx4 s[12:15], s[0:1], 0x20
	v_and_b32_e32 v1, 63, v0
	v_lshrrev_b32_e32 v2, 6, v0
	s_nop 1
	v_readfirstlane_b32 s16, v2
	s_lshr_b32 s17, s2, 7
	s_and_b32 s18, s2, 127
	s_lshl_b32 s18, s18, 2
	s_add_u32 s18, s18, s16
	s_lshl_b32 s19, s17, 9
	s_add_u32 s19, s19, s18
	s_mul_i32 s28, s16, 4608
	s_add_u32 s28, s28, 67584
	s_lshl_b32 s32, s16, 10
	s_add_u32 s33, s32, 0x1000
	s_add_u32 s34, s32, 0x2000
	s_add_u32 s35, s32, 0x3000
	s_mov_b32 s46, 0x200
	s_mov_b32 s47, 0
	s_mov_b32 s40, 0
	v_lshlrev_b32_e32 v2, 4, v1
	v_add_u32_e32 v3, 0x1000, v2
	v_add_u32_e32 v4, 0x2000, v2
	v_add_u32_e32 v5, 0x3000, v2
	v_lshlrev_b32_e32 v6, 2, v1
	v_lshlrev_b32_e32 v7, 1, v1
	v_and_b32_e32 v20, 7, v1
	v_lshlrev_b32_e32 v20, 1, v20
	v_add_u32_e32 v8, v2, v20
	v_add_u32_e32 v8, s28, v8
	v_and_b32_e32 v20, 3, v1
	v_bfe_u32 v21, v1, 3, 2
	v_lshl_add_u32 v20, v21, 2, v20
	v_lshrrev_b32_e32 v21, 5, v1
	v_bfe_u32 v22, v1, 2, 1
	v_bfe_u32 v23, v1, 4, 1
	v_cmp_eq_u32_e64 s[48:49], v21, v22
	v_cmp_eq_u32_e64 s[50:51], 0, v23
	s_nop 1
	s_and_b64 s[52:53], s[48:49], s[50:51]
	s_andn2_b64 s[54:55], s[48:49], s[50:51]
	v_mov_b32_e32 v24, 65536
	v_lshlrev_b32_e32 v25, 1, v20
	v_add_u32_e32 v25, s28, v25
	v_add_u32_e32 v26, 0x100, v25
	s_nop 1
	v_cndmask_b32_e64 v9, v24, v25, s[48:49]
	v_cndmask_b32_e64 v10, v24, v26, s[48:49]
	v_lshlrev_b32_e32 v25, 4, v20
	v_add_u32_e32 v25, s28, v25
	v_add_u32_e32 v25, 0x200, v25
	v_add_u32_e32 v26, 0x800, v25
	v_cndmask_b32_e64 v11, v24, v25, s[48:49]
	v_cndmask_b32_e64 v13, v24, v26, s[48:49]
	v_mov_b32_e32 v15, 1.0
	v_and_b32_e32 v89, 15, v1
	s_mov_b32 s42, 0xffff
	s_mov_b32 s43, 0
	v_xor_b32_e32 v86, 16, v1
	v_lshlrev_b32_e32 v86, 2, v86
	v_xor_b32_e32 v87, 32, v1
	v_lshlrev_b32_e32 v87, 2, v87
	s_waitcnt lgkmcnt(0)
	s_lshl_b32 s30, s19, 13
	s_add_u32 s24, s4, s30
	s_addc_u32 s25, s5, 0
	s_add_u32 s26, s6, s30
	s_addc_u32 s27, s7, 0
	s_lshl_b32 s30, s17, 19
	s_add_u32 s30, s30, s32
	s_add_u32 s20, s8, s30
	s_addc_u32 s21, s9, 0
	s_add_u32 s22, s10, s30
	s_addc_u32 s23, s11, 0
	s_lshl_b32 s30, s18, 8
	s_add_u32 s12, s12, s30
	s_addc_u32 s13, s13, 0
	global_load_dword v90, v6, s[12:13]
	global_load_ushort v18, v7, s[26:27]
	global_load_ushort v19, v7, s[26:27] offset:128
	s_lshl_b32 s30, s19, 14
	s_add_u32 s14, s14, s30
	s_addc_u32 s15, s15, 0
	v_and_b32_e32 v30, 15, v1
	v_lshlrev_b32_e32 v30, 2, v30
	v_mov_b32_e32 v31, 0
	v_lshl_add_u64 v[16:17], s[14:15], 0, v[30:31]
	v_mov_b32_e32 v36, 0
	v_mov_b32_e32 v37, 0
	v_mov_b32_e32 v38, 0
	v_mov_b32_e32 v39, 0
	v_add_u32_e32 v29, 65536, v2
	ds_write_b128 v29, v[36:39]
	ds_write_b128 v29, v[36:39] offset:1024
	v_add_u32_e32 v29, s28, v2
	ds_write_b128 v29, v[36:39] offset:512
	ds_write_b128 v29, v[36:39] offset:1536
	ds_write_b128 v29, v[36:39] offset:2560
	ds_write_b128 v29, v[36:39] offset:3584
	s_mov_b32 m0, s32
	s_nop 0
	global_load_lds_dwordx4 v2, s[20:21]
	s_add_i32 m0, s32, 32768
	s_nop 0
	global_load_lds_dwordx4 v2, s[22:23]
	s_mov_b32 m0, s33
	s_nop 0
	global_load_lds_dwordx4 v3, s[20:21]
	s_add_i32 m0, s33, 32768
	s_nop 0
	global_load_lds_dwordx4 v3, s[22:23]
	s_mov_b32 m0, s34
	s_nop 0
	global_load_lds_dwordx4 v4, s[20:21]
	s_add_i32 m0, s34, 32768
	s_nop 0
	global_load_lds_dwordx4 v4, s[22:23]
	s_mov_b32 m0, s35
	s_nop 0
	global_load_lds_dwordx4 v5, s[20:21]
	s_add_i32 m0, s35, 32768
	s_nop 0
	global_load_lds_dwordx4 v5, s[22:23]
	s_mov_b32 m0, s28
	s_nop 0
	global_load_lds_dword v6, s[24:25]
	s_add_u32 s20, s20, 0x4000
	s_addc_u32 s21, s21, 0
	s_add_u32 s22, s22, 0x4000
	s_addc_u32 s23, s23, 0
	s_add_u32 s24, s24, 0x100
	s_addc_u32 s25, s25, 0
	s_add_i32 m0, s32, 16384
	s_nop 0
	global_load_lds_dwordx4 v2, s[20:21]
	s_add_i32 m0, s32, 49152
	s_nop 0
	global_load_lds_dwordx4 v2, s[22:23]
	s_add_i32 m0, s33, 16384
	s_nop 0
	global_load_lds_dwordx4 v3, s[20:21]
	s_add_i32 m0, s33, 49152
	s_nop 0
	global_load_lds_dwordx4 v3, s[22:23]
	s_add_i32 m0, s34, 16384
	s_nop 0
	global_load_lds_dwordx4 v4, s[20:21]
	s_add_i32 m0, s34, 49152
	s_nop 0
	global_load_lds_dwordx4 v4, s[22:23]
	s_add_i32 m0, s35, 16384
	s_nop 0
	global_load_lds_dwordx4 v5, s[20:21]
	s_add_i32 m0, s35, 49152
	s_nop 0
	global_load_lds_dwordx4 v5, s[22:23]
	s_add_i32 m0, s28, 0x100
	s_nop 0
	global_load_lds_dword v6, s[24:25]
	s_add_u32 s20, s20, 0x4000
	s_addc_u32 s21, s21, 0
	s_add_u32 s22, s22, 0x4000
	s_addc_u32 s23, s23, 0
	s_add_u32 s24, s24, 0x100
	s_addc_u32 s25, s25, 0
	s_mov_b32 s3, 0x3fb8aa3b
	s_waitcnt vmcnt(20)
	v_mul_f32_e32 v91, 0x3fb8aa3b, v90
	v_fma_f32 v92, v90, s3, -v91
	v_rndne_f32_e32 v93, v91
	v_fmamk_f32 v92, v90, 0x32a5705f, v92
	v_sub_f32_e32 v91, v91, v93
	v_add_f32_e32 v91, v91, v92
	v_exp_f32_e32 v91, v91
	v_cvt_i32_f32_e32 v92, v93
	s_mov_b32 s3, 0xc2ce8ed0
	v_cmp_ngt_f32_e32 vcc, s3, v90
	s_mov_b32 s3, 0x42b17218
	v_ldexp_f32 v91, v91, v92
	v_cndmask_b32_e32 v91, 0, v91, vcc
	v_mov_b32_e32 v92, 0x7f800000
	v_cmp_nlt_f32_e32 vcc, s3, v90
	s_mov_b32 s3, 0xbfb8aa3b
	s_nop 1
	v_cndmask_b32_e32 v90, v92, v91, vcc
	v_mov_b32_e32 v93, 0
	s_nop 0
	v_fma_mixlo_f16 v93, v90, s3, 0
	v_and_b32_e32 v28, 0xffff, v93
	v_mov_b32_e32 v29, 0
	v_mov_b32_e32 v30, 0
	v_mov_b32_e32 v31, 0
	v_mov_b32_e32 v32, 0
	v_mov_b32_e32 v33, 0
	v_mov_b32_e32 v34, 0
	v_mov_b32_e32 v35, 0
	v_mov_b32_e32 v96, 0x1c00
	v_mov_b32_e32 v97, 0x1c000000
	v_cmp_eq_u32_e32 vcc, 0, v89
	s_nop 1
	v_cndmask_b32_e32 v20, 0, v96, vcc
	v_cmp_eq_u32_e32 vcc, 1, v89
	s_nop 1
	v_cndmask_b32_e32 v20, v20, v97, vcc
	v_cmp_eq_u32_e32 vcc, 2, v89
	s_nop 1
	v_cndmask_b32_e32 v21, 0, v96, vcc
	v_cmp_eq_u32_e32 vcc, 3, v89
	s_nop 1
	v_cndmask_b32_e32 v21, v21, v97, vcc
	v_cmp_eq_u32_e32 vcc, 4, v89
	s_nop 1
	v_cndmask_b32_e32 v22, 0, v96, vcc
	v_cmp_eq_u32_e32 vcc, 5, v89
	s_nop 1
	v_cndmask_b32_e32 v22, v22, v97, vcc
	v_cmp_eq_u32_e32 vcc, 6, v89
	s_nop 1
	v_cndmask_b32_e32 v23, 0, v96, vcc
	v_cmp_eq_u32_e32 vcc, 7, v89
	s_nop 1
	v_cndmask_b32_e32 v23, v23, v97, vcc
	v_cmp_eq_u32_e32 vcc, 8, v89
	s_nop 1
	v_cndmask_b32_e32 v24, 0, v96, vcc
	v_cmp_eq_u32_e32 vcc, 9, v89
	s_nop 1
	v_cndmask_b32_e32 v24, v24, v97, vcc
	v_cmp_eq_u32_e32 vcc, 10, v89
	s_nop 1
	v_cndmask_b32_e32 v25, 0, v96, vcc
	v_cmp_eq_u32_e32 vcc, 11, v89
	s_nop 1
	v_cndmask_b32_e32 v25, v25, v97, vcc
	v_cmp_eq_u32_e32 vcc, 12, v89
	s_nop 1
	v_cndmask_b32_e32 v26, 0, v96, vcc
	v_cmp_eq_u32_e32 vcc, 13, v89
	s_nop 1
	v_cndmask_b32_e32 v26, v26, v97, vcc
	v_cmp_eq_u32_e32 vcc, 14, v89
	s_nop 1
	v_cndmask_b32_e32 v27, 0, v96, vcc
	v_cmp_eq_u32_e32 vcc, 15, v89
	s_nop 1
	v_cndmask_b32_e32 v27, v27, v97, vcc
	v_mov_b32_e32 v195, 0
	v_mov_b32_e32 v85, 0
	v_mov_b32_e32 v88, 0
	v_mov_b32_e32 v84, 0
	v_mov_b32_e32 v68, 0
	v_mov_b32_e32 v69, 0
	v_mov_b32_e32 v70, 0
	v_mov_b32_e32 v71, 0
	v_mov_b32_e32 v72, 0
	v_mov_b32_e32 v73, 0
	v_mov_b32_e32 v74, 0
	v_mov_b32_e32 v75, 0
	v_mov_b32_e32 v76, 0
	v_mov_b32_e32 v77, 0
	v_mov_b32_e32 v78, 0
	v_mov_b32_e32 v79, 0
	v_mov_b32_e32 v80, 0
	v_mov_b32_e32 v81, 0
	v_mov_b32_e32 v82, 0
	v_mov_b32_e32 v83, 0
	s_waitcnt vmcnt(18)
	v_add_u32_e32 v8, 0x200, v8
	v_add_u32_e32 v94, 0x800, v8
	v_mov_b32_e32 v92, v2
	v_add_u32_e32 v93, 0x4000, v2
	s_mov_b32 s29, s28
	ds_write_b16 v8, v18
	ds_write_b16 v8, v19 offset:1024
	s_add_u32 s26, s26, 0x100
	s_addc_u32 s27, s27, 0
	global_load_ushort v18, v7, s[26:27]
	global_load_ushort v19, v7, s[26:27] offset:128
	s_add_u32 s26, s26, 0x100
	s_addc_u32 s27, s27, 0
	s_waitcnt vmcnt(0)
	s_waitcnt lgkmcnt(0)
	s_barrier
	ds_read_b128 v[52:55], v92 offset:32768
	ds_read_b128 v[56:59], v92 offset:33792
	ds_read_u16 v32, v9 offset:0
	ds_read_b128 v[36:39], v11 offset:0
	ds_read_b128 v[44:47], v92 offset:0
	ds_read_b128 v[48:51], v92 offset:1024
	s_waitcnt lgkmcnt(0)
	v_mfma_f32_32x32x8_f16 v[98:113], v[32:33], v[28:29], 0
	v_mfma_f32_32x32x16_f16 v[132:147], v[36:39], v[44:47], 0
	v_mfma_f32_32x32x16_f16 v[164:179], v[36:39], v[48:51], 0
	ds_read_u16 v32, v9 offset:32
	ds_read_b128 v[36:39], v11 offset:256
	ds_read_b128 v[44:47], v92 offset:2048
	ds_read_b128 v[48:51], v92 offset:3072
	s_nop 15
	s_nop 15
.Lscan_loop:
	v_exp_f32_e32 v98, v98
	v_exp_f32_e32 v99, v99
	v_mfma_f32_16x16x32_f16 v[80:83], v[72:75], v[24:27], v[80:83]
	ds_read_b128 v[60:63], v92 offset:34816
	ds_bpermute_b32 v90, v87, v85
	s_waitcnt lgkmcnt(2)
	v_exp_f32_e32 v100, v100
	v_exp_f32_e32 v101, v101
	v_mfma_f32_32x32x8_f16 v[114:129], v[32:33], v[28:29], 0
	ds_read_u16 v32, v9 offset:64
	ds_read_b128 v[64:67], v92 offset:35840
	v_fmac_f32_e32 v132, v98, v195
	v_exp_f32_e32 v102, v102
	v_fmac_f32_e32 v133, v99, v132
	v_exp_f32_e32 v103, v103
	v_fmac_f32_e32 v134, v100, v133
	v_cvt_pkrtz_f16_f32 v68, v132, v133
	v_exp_f32_e32 v104, v104
	v_fmac_f32_e32 v135, v101, v134
	v_pk_mul_f16 v68, v52, v68
	v_exp_f32_e32 v105, v105
	v_add_f32_e32 v84, v80, v81
	v_add_f32_e32 v91, v82, v83
	v_fmac_f32_e32 v136, v102, v135
	v_add_f32_e32 v84, v84, v91
	v_cvt_pkrtz_f16_f32 v69, v134, v135
	v_mfma_f32_32x32x16_f16 v[148:163], v[36:39], v[44:47], 0
	ds_read_b128 v[44:47], v92 offset:4096
	ds_bpermute_b32 v89, v86, v84
	v_exp_f32_e32 v106, v106
	v_fmac_f32_e32 v137, v103, v136
	v_pk_mul_f16 v69, v53, v69
	v_exp_f32_e32 v107, v107
	v_fmac_f32_e32 v138, v104, v137
	v_cvt_pkrtz_f16_f32 v70, v136, v137
	v_exp_f32_e32 v108, v108
	v_fmac_f32_e32 v139, v105, v138
	v_pk_mul_f16 v70, v54, v70
	v_exp_f32_e32 v109, v109
	v_mfma_f32_32x32x16_f16 v[180:195], v[36:39], v[48:51], 0
	ds_read_b128 v[36:39], v11 offset:512
	ds_read_b128 v[48:51], v92 offset:5120
	v_cvt_pkrtz_f16_f32 v71, v138, v139
	v_fmac_f32_e32 v172, v106, v139
	v_pk_mul_f16 v71, v55, v71
	v_exp_f32_e32 v110, v110
	v_fmac_f32_e32 v173, v107, v172
	v_mfma_f32_16x16x32_f16 v[76:79], v[68:71], v[20:23], 0
	v_cvt_pkrtz_f16_f32 v72, v172, v173
	v_exp_f32_e32 v111, v111
	v_fmac_f32_e32 v174, v108, v173
	v_pk_mul_f16 v72, v56, v72
	v_fmac_f32_e32 v175, v109, v174
	v_exp_f32_e32 v112, v112
	v_cvt_pkrtz_f16_f32 v73, v174, v175
	v_fmac_f32_e32 v176, v110, v175
	v_pk_mul_f16 v73, v57, v73
	v_fmac_f32_e32 v177, v111, v176
	v_exp_f32_e32 v113, v113
	v_cvt_pkrtz_f16_f32 v74, v176, v177
	v_fmac_f32_e32 v178, v112, v177
	v_pk_mul_f16 v74, v58, v74
	s_waitcnt lgkmcnt(2)
	v_add_f32_e32 v202, v85, v90
	v_fmac_f32_e32 v179, v113, v178
	v_add_f32_e32 v88, v84, v89
	v_cvt_pkrtz_f16_f32 v75, v178, v179
	v_pk_mul_f16 v75, v59, v75
	v_exp_f32_e32 v114, v114
	v_exp_f32_e32 v115, v115
	v_mfma_f32_16x16x32_f16 v[76:79], v[72:75], v[24:27], v[76:79]
	ds_read_b128 v[52:55], v92 offset:36864
	ds_bpermute_b32 v90, v87, v88
	s_waitcnt lgkmcnt(2)
	v_exp_f32_e32 v116, v116
	v_exp_f32_e32 v117, v117
	v_mfma_f32_32x32x8_f16 v[98:113], v[32:33], v[28:29], 0
	ds_read_u16 v32, v9 offset:96
	ds_read_b128 v[56:59], v92 offset:37888
	v_fmac_f32_e32 v148, v114, v179
	v_exp_f32_e32 v118, v118
	v_fmac_f32_e32 v149, v115, v148
	v_exp_f32_e32 v119, v119
	v_fmac_f32_e32 v150, v116, v149
	v_cvt_pkrtz_f16_f32 v68, v148, v149
	v_exp_f32_e32 v120, v120
	v_fmac_f32_e32 v151, v117, v150
	v_pk_mul_f16 v68, v60, v68
	v_exp_f32_e32 v121, v121
	v_add_f32_e32 v84, v76, v77
	v_add_f32_e32 v91, v78, v79
	v_fmac_f32_e32 v152, v118, v151
	v_add_f32_e32 v84, v84, v91
	v_cvt_pkrtz_f16_f32 v69, v150, v151
	v_mfma_f32_32x32x16_f16 v[132:147], v[36:39], v[44:47], 0
	ds_read_b128 v[44:47], v92 offset:6144
	ds_bpermute_b32 v89, v86, v84
	v_exp_f32_e32 v122, v122
	v_fmac_f32_e32 v153, v119, v152
	v_pk_mul_f16 v69, v61, v69
	v_exp_f32_e32 v123, v123
	v_fmac_f32_e32 v154, v120, v153
	v_cvt_pkrtz_f16_f32 v70, v152, v153
	v_exp_f32_e32 v124, v124
	v_fmac_f32_e32 v155, v121, v154
	v_pk_mul_f16 v70, v62, v70
	v_exp_f32_e32 v125, v125
	v_mfma_f32_32x32x16_f16 v[164:179], v[36:39], v[48:51], 0
	ds_read_b128 v[36:39], v11 offset:768
	ds_read_b128 v[48:51], v92 offset:7168
	v_cvt_pkrtz_f16_f32 v71, v154, v155
	v_fmac_f32_e32 v188, v122, v155
	v_pk_mul_f16 v71, v63, v71
	v_exp_f32_e32 v126, v126
	v_fmac_f32_e32 v189, v123, v188
	v_mfma_f32_16x16x32_f16 v[80:83], v[68:71], v[20:23], 0
	v_cvt_pkrtz_f16_f32 v72, v188, v189
	v_exp_f32_e32 v127, v127
	v_fmac_f32_e32 v190, v124, v189
	v_pk_mul_f16 v72, v64, v72
	v_fmac_f32_e32 v191, v125, v190
	v_exp_f32_e32 v128, v128
	v_cvt_pkrtz_f16_f32 v73, v190, v191
	v_fmac_f32_e32 v192, v126, v191
	v_pk_mul_f16 v73, v65, v73
	v_fmac_f32_e32 v193, v127, v192
	v_exp_f32_e32 v129, v129
	v_cvt_pkrtz_f16_f32 v74, v192, v193
	v_fmac_f32_e32 v194, v128, v193
	v_pk_mul_f16 v74, v66, v74
	s_waitcnt lgkmcnt(2)
	v_add_f32_e32 v203, v88, v90
	v_fmac_f32_e32 v195, v129, v194
	v_add_f32_e32 v85, v84, v89
	v_cvt_pkrtz_f16_f32 v75, v194, v195
	v_pk_mul_f16 v75, v67, v75
	v_exp_f32_e32 v98, v98
	v_exp_f32_e32 v99, v99
	v_mfma_f32_16x16x32_f16 v[80:83], v[72:75], v[24:27], v[80:83]
	ds_read_b128 v[60:63], v92 offset:38912
	ds_bpermute_b32 v90, v87, v85
	s_waitcnt lgkmcnt(2)
	v_exp_f32_e32 v100, v100
	v_exp_f32_e32 v101, v101
	v_mfma_f32_32x32x8_f16 v[114:129], v[32:33], v[28:29], 0
	ds_read_u16 v32, v9 offset:128
	ds_read_b128 v[64:67], v92 offset:39936
	v_fmac_f32_e32 v132, v98, v195
	v_exp_f32_e32 v102, v102
	v_fmac_f32_e32 v133, v99, v132
	v_exp_f32_e32 v103, v103
	v_fmac_f32_e32 v134, v100, v133
	v_cvt_pkrtz_f16_f32 v68, v132, v133
	v_exp_f32_e32 v104, v104
	v_fmac_f32_e32 v135, v101, v134
	v_pk_mul_f16 v68, v52, v68
	v_exp_f32_e32 v105, v105
	v_add_f32_e32 v84, v80, v81
	v_add_f32_e32 v91, v82, v83
	v_fmac_f32_e32 v136, v102, v135
	v_add_f32_e32 v84, v84, v91
	v_cvt_pkrtz_f16_f32 v69, v134, v135
	v_mfma_f32_32x32x16_f16 v[148:163], v[36:39], v[44:47], 0
	ds_read_b128 v[44:47], v92 offset:8192
	ds_bpermute_b32 v89, v86, v84
	v_exp_f32_e32 v106, v106
	v_fmac_f32_e32 v137, v103, v136
	v_pk_mul_f16 v69, v53, v69
	v_exp_f32_e32 v107, v107
	v_fmac_f32_e32 v138, v104, v137
	v_cvt_pkrtz_f16_f32 v70, v136, v137
	v_exp_f32_e32 v108, v108
	v_fmac_f32_e32 v139, v105, v138
	v_pk_mul_f16 v70, v54, v70
	v_exp_f32_e32 v109, v109
	v_mfma_f32_32x32x16_f16 v[180:195], v[36:39], v[48:51], 0
	ds_read_b128 v[36:39], v11 offset:1024
	ds_read_b128 v[48:51], v92 offset:9216
	v_cvt_pkrtz_f16_f32 v71, v138, v139
	v_fmac_f32_e32 v172, v106, v139
	v_pk_mul_f16 v71, v55, v71
	v_exp_f32_e32 v110, v110
	v_fmac_f32_e32 v173, v107, v172
	v_mfma_f32_16x16x32_f16 v[76:79], v[68:71], v[20:23], 0
	v_cvt_pkrtz_f16_f32 v72, v172, v173
	v_exp_f32_e32 v111, v111
	v_fmac_f32_e32 v174, v108, v173
	v_pk_mul_f16 v72, v56, v72
	v_fmac_f32_e32 v175, v109, v174
	v_exp_f32_e32 v112, v112
	v_cvt_pkrtz_f16_f32 v73, v174, v175
	v_fmac_f32_e32 v176, v110, v175
	v_pk_mul_f16 v73, v57, v73
	v_fmac_f32_e32 v177, v111, v176
	v_exp_f32_e32 v113, v113
	v_cvt_pkrtz_f16_f32 v74, v176, v177
	v_fmac_f32_e32 v178, v112, v177
	v_pk_mul_f16 v74, v58, v74
	s_waitcnt lgkmcnt(2)
	v_add_f32_e32 v196, v85, v90
	v_fmac_f32_e32 v179, v113, v178
	v_add_f32_e32 v88, v84, v89
	v_cvt_pkrtz_f16_f32 v75, v178, v179
	v_pk_mul_f16 v75, v59, v75
	v_exp_f32_e32 v114, v114
	v_exp_f32_e32 v115, v115
	v_mfma_f32_16x16x32_f16 v[76:79], v[72:75], v[24:27], v[76:79]
	ds_read_b128 v[52:55], v92 offset:40960
	ds_bpermute_b32 v90, v87, v88
	s_waitcnt lgkmcnt(2)
	v_exp_f32_e32 v116, v116
	v_exp_f32_e32 v117, v117
	v_mfma_f32_32x32x8_f16 v[98:113], v[32:33], v[28:29], 0
	ds_read_u16 v32, v9 offset:160
	ds_read_b128 v[56:59], v92 offset:41984
	v_fmac_f32_e32 v148, v114, v179
	v_exp_f32_e32 v118, v118
	v_fmac_f32_e32 v149, v115, v148
	v_exp_f32_e32 v119, v119
	v_fmac_f32_e32 v150, v116, v149
	v_cvt_pkrtz_f16_f32 v68, v148, v149
	v_exp_f32_e32 v120, v120
	v_fmac_f32_e32 v151, v117, v150
	v_pk_mul_f16 v68, v60, v68
	v_exp_f32_e32 v121, v121
	v_add_f32_e32 v84, v76, v77
	v_add_f32_e32 v91, v78, v79
	v_fmac_f32_e32 v152, v118, v151
	v_add_f32_e32 v84, v84, v91
	v_cvt_pkrtz_f16_f32 v69, v150, v151
	v_mfma_f32_32x32x16_f16 v[132:147], v[36:39], v[44:47], 0
	ds_read_b128 v[44:47], v92 offset:10240
	ds_bpermute_b32 v89, v86, v84
	v_exp_f32_e32 v122, v122
	v_fmac_f32_e32 v153, v119, v152
	v_pk_mul_f16 v69, v61, v69
	v_exp_f32_e32 v123, v123
	v_fmac_f32_e32 v154, v120, v153
	v_cvt_pkrtz_f16_f32 v70, v152, v153
	v_exp_f32_e32 v124, v124
	v_fmac_f32_e32 v155, v121, v154
	v_pk_mul_f16 v70, v62, v70
	v_exp_f32_e32 v125, v125
	v_mfma_f32_32x32x16_f16 v[164:179], v[36:39], v[48:51], 0
	ds_read_b128 v[36:39], v11 offset:1280
	ds_read_b128 v[48:51], v92 offset:11264
	v_cvt_pkrtz_f16_f32 v71, v154, v155
	v_fmac_f32_e32 v188, v122, v155
	v_pk_mul_f16 v71, v63, v71
	v_exp_f32_e32 v126, v126
	v_fmac_f32_e32 v189, v123, v188
	v_mfma_f32_16x16x32_f16 v[80:83], v[68:71], v[20:23], 0
	v_cvt_pkrtz_f16_f32 v72, v188, v189
	v_exp_f32_e32 v127, v127
	v_fmac_f32_e32 v190, v124, v189
	v_pk_mul_f16 v72, v64, v72
	v_fmac_f32_e32 v191, v125, v190
	v_exp_f32_e32 v128, v128
	v_cvt_pkrtz_f16_f32 v73, v190, v191
	v_fmac_f32_e32 v192, v126, v191
	v_pk_mul_f16 v73, v65, v73
	v_fmac_f32_e32 v193, v127, v192
	v_exp_f32_e32 v129, v129
	v_cvt_pkrtz_f16_f32 v74, v192, v193
	v_fmac_f32_e32 v194, v128, v193
	v_pk_mul_f16 v74, v66, v74
	s_waitcnt lgkmcnt(2)
	v_add_f32_e32 v197, v88, v90
	v_fmac_f32_e32 v195, v129, v194
	v_add_f32_e32 v85, v84, v89
	v_cvt_pkrtz_f16_f32 v75, v194, v195
	v_pk_mul_f16 v75, v67, v75
	v_exp_f32_e32 v98, v98
	v_exp_f32_e32 v99, v99
	v_mfma_f32_16x16x32_f16 v[80:83], v[72:75], v[24:27], v[80:83]
	ds_read_b128 v[60:63], v92 offset:43008
	ds_bpermute_b32 v90, v87, v85
	s_waitcnt lgkmcnt(2)
	v_exp_f32_e32 v100, v100
	v_exp_f32_e32 v101, v101
	v_mfma_f32_32x32x8_f16 v[114:129], v[32:33], v[28:29], 0
	ds_read_u16 v32, v9 offset:192
	ds_read_b128 v[64:67], v92 offset:44032
	v_fmac_f32_e32 v132, v98, v195
	v_exp_f32_e32 v102, v102
	v_fmac_f32_e32 v133, v99, v132
	v_exp_f32_e32 v103, v103
	v_fmac_f32_e32 v134, v100, v133
	v_cvt_pkrtz_f16_f32 v68, v132, v133
	v_exp_f32_e32 v104, v104
	v_fmac_f32_e32 v135, v101, v134
	v_pk_mul_f16 v68, v52, v68
	v_exp_f32_e32 v105, v105
	v_add_f32_e32 v84, v80, v81
	v_add_f32_e32 v91, v82, v83
	v_fmac_f32_e32 v136, v102, v135
	v_add_f32_e32 v84, v84, v91
	v_cvt_pkrtz_f16_f32 v69, v134, v135
	v_mfma_f32_32x32x16_f16 v[148:163], v[36:39], v[44:47], 0
	ds_read_b128 v[44:47], v92 offset:12288
	ds_bpermute_b32 v89, v86, v84
	v_exp_f32_e32 v106, v106
	v_fmac_f32_e32 v137, v103, v136
	v_pk_mul_f16 v69, v53, v69
	v_exp_f32_e32 v107, v107
	v_fmac_f32_e32 v138, v104, v137
	v_cvt_pkrtz_f16_f32 v70, v136, v137
	v_exp_f32_e32 v108, v108
	v_fmac_f32_e32 v139, v105, v138
	v_pk_mul_f16 v70, v54, v70
	v_exp_f32_e32 v109, v109
	v_mfma_f32_32x32x16_f16 v[180:195], v[36:39], v[48:51], 0
	ds_read_b128 v[36:39], v11 offset:1536
	ds_read_b128 v[48:51], v92 offset:13312
	v_cvt_pkrtz_f16_f32 v71, v138, v139
	v_fmac_f32_e32 v172, v106, v139
	v_pk_mul_f16 v71, v55, v71
	v_exp_f32_e32 v110, v110
	v_fmac_f32_e32 v173, v107, v172
	v_mfma_f32_16x16x32_f16 v[76:79], v[68:71], v[20:23], 0
	v_cvt_pkrtz_f16_f32 v72, v172, v173
	v_exp_f32_e32 v111, v111
	v_fmac_f32_e32 v174, v108, v173
	v_pk_mul_f16 v72, v56, v72
	v_fmac_f32_e32 v175, v109, v174
	v_exp_f32_e32 v112, v112
	v_cvt_pkrtz_f16_f32 v73, v174, v175
	v_fmac_f32_e32 v176, v110, v175
	v_pk_mul_f16 v73, v57, v73
	v_fmac_f32_e32 v177, v111, v176
	v_exp_f32_e32 v113, v113
	v_cvt_pkrtz_f16_f32 v74, v176, v177
	v_fmac_f32_e32 v178, v112, v177
	v_pk_mul_f16 v74, v58, v74
	s_waitcnt lgkmcnt(2)
	v_add_f32_e32 v198, v85, v90
	v_fmac_f32_e32 v179, v113, v178
	v_add_f32_e32 v88, v84, v89
	v_cvt_pkrtz_f16_f32 v75, v178, v179
	v_pk_mul_f16 v75, v59, v75
	v_exp_f32_e32 v114, v114
	v_exp_f32_e32 v115, v115
	v_mfma_f32_16x16x32_f16 v[76:79], v[72:75], v[24:27], v[76:79]
	ds_read_b128 v[52:55], v92 offset:45056
	ds_bpermute_b32 v90, v87, v88
	s_waitcnt lgkmcnt(2)
	v_exp_f32_e32 v116, v116
	v_exp_f32_e32 v117, v117
	v_mfma_f32_32x32x8_f16 v[98:113], v[32:33], v[28:29], 0
	ds_read_u16 v32, v9 offset:224
	ds_read_b128 v[56:59], v92 offset:46080
	v_fmac_f32_e32 v148, v114, v179
	v_exp_f32_e32 v118, v118
	v_fmac_f32_e32 v149, v115, v148
	v_exp_f32_e32 v119, v119
	v_fmac_f32_e32 v150, v116, v149
	v_cvt_pkrtz_f16_f32 v68, v148, v149
	v_exp_f32_e32 v120, v120
	v_fmac_f32_e32 v151, v117, v150
	v_pk_mul_f16 v68, v60, v68
	v_exp_f32_e32 v121, v121
	v_add_f32_e32 v84, v76, v77
	v_add_f32_e32 v91, v78, v79
	v_fmac_f32_e32 v152, v118, v151
	v_add_f32_e32 v84, v84, v91
	v_cvt_pkrtz_f16_f32 v69, v150, v151
	v_mfma_f32_32x32x16_f16 v[132:147], v[36:39], v[44:47], 0
	ds_read_b128 v[44:47], v92 offset:14336
	ds_bpermute_b32 v89, v86, v84
	v_exp_f32_e32 v122, v122
	v_fmac_f32_e32 v153, v119, v152
	v_pk_mul_f16 v69, v61, v69
	v_exp_f32_e32 v123, v123
	v_fmac_f32_e32 v154, v120, v153
	v_cvt_pkrtz_f16_f32 v70, v152, v153
	v_exp_f32_e32 v124, v124
	v_fmac_f32_e32 v155, v121, v154
	v_pk_mul_f16 v70, v62, v70
	v_exp_f32_e32 v125, v125
	v_mfma_f32_32x32x16_f16 v[164:179], v[36:39], v[48:51], 0
	ds_read_b128 v[36:39], v11 offset:1792
	ds_read_b128 v[48:51], v92 offset:15360
	v_cvt_pkrtz_f16_f32 v71, v154, v155
	v_fmac_f32_e32 v188, v122, v155
	v_pk_mul_f16 v71, v63, v71
	v_exp_f32_e32 v126, v126
	v_fmac_f32_e32 v189, v123, v188
	v_mfma_f32_16x16x32_f16 v[80:83], v[68:71], v[20:23], 0
	v_cvt_pkrtz_f16_f32 v72, v188, v189
	v_exp_f32_e32 v127, v127
	v_fmac_f32_e32 v190, v124, v189
	v_pk_mul_f16 v72, v64, v72
	v_fmac_f32_e32 v191, v125, v190
	v_exp_f32_e32 v128, v128
	v_cvt_pkrtz_f16_f32 v73, v190, v191
	v_fmac_f32_e32 v192, v126, v191
	v_pk_mul_f16 v73, v65, v73
	v_fmac_f32_e32 v193, v127, v192
	v_exp_f32_e32 v129, v129
	v_cvt_pkrtz_f16_f32 v74, v192, v193
	v_fmac_f32_e32 v194, v128, v193
	v_pk_mul_f16 v74, v66, v74
	s_waitcnt lgkmcnt(2)
	v_add_f32_e32 v199, v88, v90
	v_fmac_f32_e32 v195, v129, v194
	v_add_f32_e32 v85, v84, v89
	v_cvt_pkrtz_f16_f32 v75, v194, v195
	v_pk_mul_f16 v75, v67, v75
	v_exp_f32_e32 v98, v98
	v_exp_f32_e32 v99, v99
	v_mfma_f32_16x16x32_f16 v[80:83], v[72:75], v[24:27], v[80:83]
	ds_read_b128 v[60:63], v92 offset:47104
	ds_read_b128 v[64:67], v92 offset:48128
	ds_bpermute_b32 v90, v87, v85
	s_waitcnt vmcnt(0)
	ds_write_b16 v94, v18
	ds_write_b16 v94, v19 offset:1024
	s_waitcnt lgkmcnt(0)
	s_barrier
	v_exp_f32_e32 v100, v100
	v_exp_f32_e32 v101, v101
	v_mfma_f32_32x32x8_f16 v[114:129], v[32:33], v[28:29], 0
	s_mov_b32 m0, s32
	ds_read_u16 v32, v10 offset:0
	global_load_lds_dwordx4 v2, s[20:21]
	v_fmac_f32_e32 v132, v98, v195
	v_exp_f32_e32 v102, v102
	v_fmac_f32_e32 v133, v99, v132
	v_exp_f32_e32 v103, v103
	v_fmac_f32_e32 v134, v100, v133
	v_cvt_pkrtz_f16_f32 v68, v132, v133
	v_exp_f32_e32 v104, v104
	v_fmac_f32_e32 v135, v101, v134
	v_pk_mul_f16 v68, v52, v68
	v_exp_f32_e32 v105, v105
	v_add_f32_e32 v84, v80, v81
	v_add_f32_e32 v91, v82, v83
	v_fmac_f32_e32 v136, v102, v135
	v_add_f32_e32 v84, v84, v91
	v_cvt_pkrtz_f16_f32 v69, v134, v135
	v_mfma_f32_32x32x16_f16 v[148:163], v[36:39], v[44:47], 0
	ds_read_b128 v[44:47], v93 offset:0
	ds_bpermute_b32 v89, v86, v84
	s_add_i32 m0, s32, 32768
	s_nop 0
	global_load_lds_dwordx4 v2, s[22:23]
	v_exp_f32_e32 v106, v106
	v_fmac_f32_e32 v137, v103, v136
	v_pk_mul_f16 v69, v53, v69
	v_exp_f32_e32 v107, v107
	v_fmac_f32_e32 v138, v104, v137
	v_cvt_pkrtz_f16_f32 v70, v136, v137
	v_exp_f32_e32 v108, v108
	v_fmac_f32_e32 v139, v105, v138
	v_pk_mul_f16 v70, v54, v70
	v_exp_f32_e32 v109, v109
	v_mfma_f32_32x32x16_f16 v[180:195], v[36:39], v[48:51], 0
	ds_read_b128 v[36:39], v13 offset:0
	s_mov_b32 m0, s33
	ds_read_b128 v[48:51], v93 offset:1024
	global_load_lds_dwordx4 v3, s[20:21]
	v_cvt_pkrtz_f16_f32 v71, v138, v139
	v_fmac_f32_e32 v172, v106, v139
	v_pk_mul_f16 v71, v55, v71
	v_exp_f32_e32 v110, v110
	v_fmac_f32_e32 v173, v107, v172
	v_mfma_f32_16x16x32_f16 v[76:79], v[68:71], v[20:23], 0
	s_add_i32 m0, s33, 32768
	s_nop 0
	global_load_lds_dwordx4 v3, s[22:23]
	v_cvt_pkrtz_f16_f32 v72, v172, v173
	v_exp_f32_e32 v111, v111
	v_fmac_f32_e32 v174, v108, v173
	v_pk_mul_f16 v72, v56, v72
	v_fmac_f32_e32 v175, v109, v174
	v_exp_f32_e32 v112, v112
	v_cvt_pkrtz_f16_f32 v73, v174, v175
	v_fmac_f32_e32 v176, v110, v175
	v_pk_mul_f16 v73, v57, v73
	v_fmac_f32_e32 v177, v111, v176
	v_exp_f32_e32 v113, v113
	v_cvt_pkrtz_f16_f32 v74, v176, v177
	v_fmac_f32_e32 v178, v112, v177
	v_pk_mul_f16 v74, v58, v74
	s_waitcnt lgkmcnt(2)
	v_add_f32_e32 v200, v85, v90
	v_fmac_f32_e32 v179, v113, v178
	v_add_f32_e32 v88, v84, v89
	v_cvt_pkrtz_f16_f32 v75, v178, v179
	v_pk_mul_f16 v75, v59, v75
	v_exp_f32_e32 v114, v114
	v_exp_f32_e32 v115, v115
	v_mfma_f32_16x16x32_f16 v[76:79], v[72:75], v[24:27], v[76:79]
	s_mov_b32 m0, s34
	ds_read_b128 v[52:55], v93 offset:32768
	global_load_lds_dwordx4 v4, s[20:21]
	ds_bpermute_b32 v90, v87, v88
	s_waitcnt lgkmcnt(2)
	v_exp_f32_e32 v116, v116
	v_exp_f32_e32 v117, v117
	v_mfma_f32_32x32x8_f16 v[98:113], v[32:33], v[28:29], 0
	ds_read_u16 v32, v10 offset:32
	s_add_i32 m0, s34, 32768
	ds_read_b128 v[56:59], v93 offset:33792
	global_load_lds_dwordx4 v4, s[22:23]
	v_fmac_f32_e32 v148, v114, v179
	v_exp_f32_e32 v118, v118
	v_fmac_f32_e32 v149, v115, v148
	v_exp_f32_e32 v119, v119
	v_fmac_f32_e32 v150, v116, v149
	v_cvt_pkrtz_f16_f32 v68, v148, v149
	v_exp_f32_e32 v120, v120
	v_fmac_f32_e32 v151, v117, v150
	v_pk_mul_f16 v68, v60, v68
	v_exp_f32_e32 v121, v121
	v_add_f32_e32 v84, v76, v77
	v_add_f32_e32 v91, v78, v79
	v_fmac_f32_e32 v152, v118, v151
	v_add_f32_e32 v84, v84, v91
	v_cvt_pkrtz_f16_f32 v69, v150, v151
	v_mfma_f32_32x32x16_f16 v[132:147], v[36:39], v[44:47], 0
	ds_read_b128 v[44:47], v93 offset:2048
	ds_bpermute_b32 v89, v86, v84
	s_cmp_eq_u32 s40, 0
	s_cselect_b64 s[56:57], 0, s[42:43]
	s_and_saveexec_b64 s[44:45], s[56:57]
	global_store_dword v[16:17], v201, off offset:-192
	global_store_dword v[16:17], v202, off offset:-128
	global_store_dword v[16:17], v203, off offset:-64
	s_and_b64 exec, s[44:45], s[42:43]
	global_store_dword v[16:17], v196, off
	global_store_dword v[16:17], v197, off offset:64
	global_store_dword v[16:17], v198, off offset:128
	global_store_dword v[16:17], v199, off offset:192
	global_store_dword v[16:17], v200, off offset:256
	s_mov_b64 exec, s[44:45]
	v_exp_f32_e32 v122, v122
	v_fmac_f32_e32 v153, v119, v152
	v_pk_mul_f16 v69, v61, v69
	v_exp_f32_e32 v123, v123
	v_fmac_f32_e32 v154, v120, v153
	v_cvt_pkrtz_f16_f32 v70, v152, v153
	v_exp_f32_e32 v124, v124
	v_fmac_f32_e32 v155, v121, v154
	v_pk_mul_f16 v70, v62, v70
	v_exp_f32_e32 v125, v125
	v_mfma_f32_32x32x16_f16 v[164:179], v[36:39], v[48:51], 0
	ds_read_b128 v[36:39], v13 offset:256
	s_mov_b32 m0, s35
	ds_read_b128 v[48:51], v93 offset:3072
	global_load_lds_dwordx4 v5, s[20:21]
	s_add_i32 m0, s35, 32768
	s_nop 0
	global_load_lds_dwordx4 v5, s[22:23]
	v_cvt_pkrtz_f16_f32 v71, v154, v155
	v_fmac_f32_e32 v188, v122, v155
	v_pk_mul_f16 v71, v63, v71
	v_exp_f32_e32 v126, v126
	v_fmac_f32_e32 v189, v123, v188
	v_mfma_f32_16x16x32_f16 v[80:83], v[68:71], v[20:23], 0
	s_mov_b32 m0, s29
	s_nop 0
	global_load_lds_dword v6, s[24:25]
	global_load_ushort v18, v7, s[26:27]
	global_load_ushort v19, v7, s[26:27] offset:128
	v_cvt_pkrtz_f16_f32 v72, v188, v189
	v_exp_f32_e32 v127, v127
	v_fmac_f32_e32 v190, v124, v189
	v_pk_mul_f16 v72, v64, v72
	v_fmac_f32_e32 v191, v125, v190
	v_exp_f32_e32 v128, v128
	v_cvt_pkrtz_f16_f32 v73, v190, v191
	v_fmac_f32_e32 v192, v126, v191
	v_pk_mul_f16 v73, v65, v73
	v_fmac_f32_e32 v193, v127, v192
	v_exp_f32_e32 v129, v129
	v_cvt_pkrtz_f16_f32 v74, v192, v193
	v_fmac_f32_e32 v194, v128, v193
	v_pk_mul_f16 v74, v66, v74
	s_waitcnt lgkmcnt(2)
	v_add_f32_e32 v201, v88, v90
	v_fmac_f32_e32 v195, v129, v194
	v_add_f32_e32 v85, v84, v89
	v_cvt_pkrtz_f16_f32 v75, v194, v195
	s_cmp_lt_u32 s40, 29
	s_cselect_b32 s58, 0x4000, 0
	s_cselect_b32 s59, 0x100, 0
	s_add_u32 s20, s20, s58
	s_addc_u32 s21, s21, 0
	s_add_u32 s22, s22, s58
	s_addc_u32 s23, s23, 0
	s_add_u32 s24, s24, s59
	s_addc_u32 s25, s25, 0
	s_add_u32 s26, s26, s59
	s_addc_u32 s27, s27, 0
	v_pk_mul_f16 v75, v67, v75
	v_lshl_add_u64 v[16:17], v[16:17], 0, s[46:47]
	v_swap_b32 v92, v93
	v_swap_b32 v9, v10
	v_swap_b32 v11, v13
	v_swap_b32 v8, v94
	s_xor_b32 s32, s32, 0x4000
	s_xor_b32 s33, s33, 0x4000
	s_xor_b32 s34, s34, 0x4000
	s_xor_b32 s35, s35, 0x4000
	s_xor_b32 s29, s29, 0x100
	s_add_u32 s40, s40, 1
	s_cmp_lt_u32 s40, 32
	s_cbranch_scc1 .Lscan_loop
	s_nop 1
	v_mfma_f32_16x16x32_f16 v[80:83], v[72:75], v[24:27], v[80:83]
	ds_bpermute_b32 v90, v87, v85
	s_nop 15
	v_add_f32_e32 v84, v80, v81
	v_add_f32_e32 v91, v82, v83
	s_nop 0
	v_add_f32_e32 v84, v84, v91
	s_waitcnt lgkmcnt(0)
	v_add_f32_e32 v202, v85, v90
	ds_bpermute_b32 v89, v86, v84
	s_waitcnt lgkmcnt(0)
	v_add_f32_e32 v88, v84, v89
	s_nop 0
	ds_bpermute_b32 v90, v87, v88
	s_waitcnt lgkmcnt(0)
	v_add_f32_e32 v203, v88, v90
	s_nop 1
	s_and_saveexec_b64 s[44:45], s[42:43]
	global_store_dword v[16:17], v201, off offset:-192
	global_store_dword v[16:17], v202, off offset:-128
	global_store_dword v[16:17], v203, off offset:-64
	s_waitcnt vmcnt(0)
	s_endpgm

	.amdhsa_kernel _Z6scan_kPKDF16_S0_S0_S0_PKfPf
		.amdhsa_group_segment_fixed_size 86016
		.amdhsa_private_segment_fixed_size 0
		.amdhsa_kernarg_size 48
		.amdhsa_user_sgpr_count 2
		.amdhsa_user_sgpr_dispatch_ptr 0
		.amdhsa_user_sgpr_queue_ptr 0
		.amdhsa_user_sgpr_kernarg_segment_ptr 1
		.amdhsa_user_sgpr_dispatch_id 0
		.amdhsa_user_sgpr_kernarg_preload_length 0
		.amdhsa_user_sgpr_kernarg_preload_offset 0
		.amdhsa_user_sgpr_private_segment_size 0
		.amdhsa_uses_dynamic_stack 0
		.amdhsa_enable_private_segment 0
		.amdhsa_system_sgpr_workgroup_id_x 1
		.amdhsa_system_sgpr_workgroup_id_y 0
		.amdhsa_system_sgpr_workgroup_id_z 0
		.amdhsa_system_sgpr_workgroup_info 0
		.amdhsa_system_vgpr_workitem_id 0
		.amdhsa_next_free_vgpr 204
		.amdhsa_next_free_sgpr 96
		.amdhsa_accum_offset 204
		.amdhsa_reserve_vcc 1
		.amdhsa_float_round_mode_32 0
		.amdhsa_float_round_mode_16_64 0
		.amdhsa_float_denorm_mode_32 3
		.amdhsa_float_denorm_mode_16_64 3
		.amdhsa_dx10_clamp 1
		.amdhsa_ieee_mode 1
		.amdhsa_fp16_overflow 0
		.amdhsa_tg_split 0
		.amdhsa_exception_fp_ieee_invalid_op 0
		.amdhsa_exception_fp_denorm_src 0
		.amdhsa_exception_fp_ieee_div_zero 0
		.amdhsa_exception_fp_ieee_overflow 0
		.amdhsa_exception_fp_ieee_underflow 0
		.amdhsa_exception_fp_ieee_inexact 0
		.amdhsa_exception_int_div_zero 0
	.end_amdhsa_kernel

amdhsa.kernels:
  - .agpr_count:     0
    .args:
      - .offset:         0
        .size:           152
        .value_kind:     by_value
    .group_segment_fixed_size: 7168
    .kernarg_segment_align: 8
    .kernarg_segment_size: 152
    .language:       OpenCL C
    .language_version:
      - 2
      - 0
    .max_flat_workgroup_size: 256
    .name:           _Z6prep_k5PrepP
    .private_segment_fixed_size: 0
    .sgpr_count:     70
    .sgpr_spill_count: 0
    .symbol:         _Z6prep_k5PrepP.kd
    .uniform_work_group_size: 1
    .uses_dynamic_stack: false
    .vgpr_count:     64
    .vgpr_spill_count: 0
    .wavefront_size: 64
  - .agpr_count:     0
    .args:
      - .actual_access:  read_only
        .address_space:  global
        .offset:         0
        .size:           8
        .value_kind:     global_buffer
      - .actual_access:  read_only
        .address_space:  global
        .offset:         8
        .size:           8
        .value_kind:     global_buffer
      - .actual_access:  read_only
        .address_space:  global
        .offset:         16
        .size:           8
        .value_kind:     global_buffer
      - .actual_access:  write_only
        .address_space:  global
        .offset:         24
        .size:           8
        .value_kind:     global_buffer
      - .actual_access:  write_only
        .address_space:  global
        .offset:         32
        .size:           8
        .value_kind:     global_buffer
    .group_segment_fixed_size: 9216
    .kernarg_segment_align: 8
    .kernarg_segment_size: 40
    .language:       OpenCL C
    .language_version:
      - 2
      - 0
    .max_flat_workgroup_size: 256
    .name:           _Z8conv1d_kPKDF16_PKfS2_PDF16_S3_
    .private_segment_fixed_size: 0
    .sgpr_count:     22
    .sgpr_spill_count: 0
    .symbol:         _Z8conv1d_kPKDF16_PKfS2_PDF16_S3_.kd
    .uniform_work_group_size: 1
    .uses_dynamic_stack: false
    .vgpr_count:     53
    .vgpr_spill_count: 0
    .wavefront_size: 64
  - .agpr_count:     0
    .args:
      - .actual_access:  read_only
        .address_space:  global
        .offset:         0
        .size:           8
        .value_kind:     global_buffer
      - .actual_access:  read_only
        .address_space:  global
        .offset:         8
        .size:           8
        .value_kind:     global_buffer
      - .actual_access:  read_only
        .address_space:  global
        .offset:         16
        .size:           8
        .value_kind:     global_buffer
      - .actual_access:  read_only
        .address_space:  global
        .offset:         24
        .size:           8
        .value_kind:     global_buffer
      - .actual_access:  write_only
        .address_space:  global
        .offset:         32
        .size:           8
        .value_kind:     global_buffer
      - .actual_access:  write_only
        .address_space:  global
        .offset:         40
        .size:           8
        .value_kind:     global_buffer
    .group_segment_fixed_size: 70656
    .kernarg_segment_align: 8
    .kernarg_segment_size: 48
    .language:       OpenCL C
    .language_version:
      - 2
      - 0
    .max_flat_workgroup_size: 256
    .name:           _Z4dt_kPKfS0_S0_PKDF16_PDF16_S3_
    .private_segment_fixed_size: 0
    .sgpr_count:     25
    .sgpr_spill_count: 0
    .symbol:         _Z4dt_kPKfS0_S0_PKDF16_PDF16_S3_.kd
    .uniform_work_group_size: 1
    .uses_dynamic_stack: false
    .vgpr_count:     96
    .vgpr_spill_count: 0
    .wavefront_size: 64
  - .agpr_count:     0
    .args:
      - .address_space:  global
        .offset:         0
        .size:           8
        .value_kind:     global_buffer
      - .actual_access:  read_only
        .address_space:  global
        .offset:         8
        .size:           8
        .value_kind:     global_buffer
      - .address_space:  global
        .offset:         16
        .size:           8
        .value_kind:     global_buffer
      - .address_space:  global
        .offset:         24
        .size:           8
        .value_kind:     global_buffer
      - .actual_access:  read_only
        .address_space:  global
        .offset:         32
        .size:           8
        .value_kind:     global_buffer
      - .actual_access:  write_only
        .address_space:  global
        .offset:         40
        .size:           8
        .value_kind:     global_buffer
    .group_segment_fixed_size: 86016
    .kernarg_segment_align: 8
    .kernarg_segment_size: 48
    .language:       OpenCL C
    .language_version:
      - 2
      - 0
    .max_flat_workgroup_size: 256
    .name:           _Z6scan_kPKDF16_S0_S0_S0_PKfPf
    .private_segment_fixed_size: 0
    .sgpr_count:     66
    .sgpr_spill_count: 0
    .symbol:         _Z6scan_kPKDF16_S0_S0_S0_PKfPf.kd
    .uniform_work_group_size: 1
    .uses_dynamic_stack: false
    .vgpr_count:     204
    .vgpr_spill_count: 0
    .wavefront_size: 64
  - .agpr_count:     0
    .args:
      - .actual_access:  read_only
        .address_space:  global
        .offset:         0
        .size:           8
        .value_kind:     global_buffer
      - .actual_access:  read_only
        .address_space:  global
        .offset:         8
        .size:           8
        .value_kind:     global_buffer
      - .actual_access:  read_only
        .address_space:  global
        .offset:         16
        .size:           8
        .value_kind:     global_buffer
      - .actual_access:  read_only
        .address_space:  global
        .offset:         24
        .size:           8
        .value_kind:     global_buffer
      - .actual_access:  write_only
        .address_space:  global
        .offset:         32
        .size:           8
        .value_kind:     global_buffer
    .group_segment_fixed_size: 9216
    .kernarg_segment_align: 8
    .kernarg_segment_size: 40
    .language:       OpenCL C
    .language_version:
      - 2
      - 0
    .max_flat_workgroup_size: 256
    .name:           _Z6gate_kPKfPKDF16_S2_S0_PDF16_
    .private_segment_fixed_size: 0
    .sgpr_count:     22
    .sgpr_spill_count: 0
    .symbol:         _Z6gate_kPKfPKDF16_S2_S0_PDF16_.kd
    .uniform_work_group_size: 1
    .uses_dynamic_stack: false
    .vgpr_count:     46
    .vgpr_spill_count: 0
    .wavefront_size: 64
  - .agpr_count:     0
    .args:
      - .actual_access:  read_only
        .address_space:  global
        .offset:         0
        .size:           8
        .value_kind:     global_buffer
      - .actual_access:  read_only
        .address_space:  global
        .offset:         8
        .size:           8
        .value_kind:     global_buffer
      - .actual_access:  read_only
        .address_space:  global
        .offset:         16
        .size:           8
        .value_kind:     global_buffer
      - .actual_access:  write_only
        .address_space:  global
        .offset:         24
        .size:           8
        .value_kind:     global_buffer
    .group_segment_fixed_size: 43776
    .kernarg_segment_align: 8
    .kernarg_segment_size: 32
    .language:       OpenCL C
    .language_version:
      - 2
      - 0
    .max_flat_workgroup_size: 256
    .name:           _Z9deconv3_kPKDF16_PKfS2_Pf
    .private_segment_fixed_size: 0
    .sgpr_count:     30
    .sgpr_spill_count: 0
    .symbol:         _Z9deconv3_kPKDF16_PKfS2_Pf.kd
    .uniform_work_group_size: 1
    .uses_dynamic_stack: false
    .vgpr_count:     60
    .vgpr_spill_count: 0
    .wavefront_size: 64
  - .agpr_count:     8
    .args:
      - .offset:         0
        .size:           112
        .value_kind:     by_value
    .group_segment_fixed_size: 49152
    .kernarg_segment_align: 8
    .kernarg_segment_size: 112
    .language:       OpenCL C
    .language_version:
      - 2
      - 0
    .max_flat_workgroup_size: 256
    .name:           _Z6gemm_gILi32ELi64ELi16ELi32ELi1ELi0ELi64ELi4EEv5GemmP
    .private_segment_fixed_size: 0
    .sgpr_count:     34
    .sgpr_spill_count: 0
    .symbol:         _Z6gemm_gILi32ELi64ELi16ELi32ELi1ELi0ELi64ELi4EEv5GemmP.kd
    .uniform_work_group_size: 1
    .uses_dynamic_stack: false
    .vgpr_count:     40
    .vgpr_spill_count: 0
    .wavefront_size: 64
  - .agpr_count:     16
    .args:
      - .offset:         0
        .size:           112
        .value_kind:     by_value
    .group_segment_fixed_size: 65536
    .kernarg_segment_align: 8
    .kernarg_segment_size: 112
    .language:       OpenCL C
    .language_version:
      - 2
      - 0
    .max_flat_workgroup_size: 256
    .name:           _Z6gemm_gILi64ELi64ELi32ELi32ELi1ELi0ELi64ELi4EEv5GemmP
    .private_segment_fixed_size: 0
    .sgpr_count:     34
    .sgpr_spill_count: 0
    .symbol:         _Z6gemm_gILi64ELi64ELi32ELi32ELi1ELi0ELi64ELi4EEv5GemmP.kd
    .uniform_work_group_size: 1
    .uses_dynamic_stack: false
    .vgpr_count:     56
    .vgpr_spill_count: 0
    .wavefront_size: 64
  - .agpr_count:     32
    .args:
      - .offset:         0
        .size:           112
        .value_kind:     by_value
    .group_segment_fixed_size: 73728
    .kernarg_segment_align: 8
    .kernarg_segment_size: 112
    .language:       OpenCL C
    .language_version:
      - 2
      - 0
    .max_flat_workgroup_size: 256
    .name:           _Z6gemm_gILi64ELi128ELi32ELi64ELi0ELi2ELi64ELi3EEv5GemmP
    .private_segment_fixed_size: 0
    .sgpr_count:     27
    .sgpr_spill_count: 0
    .symbol:         _Z6gemm_gILi64ELi128ELi32ELi64ELi0ELi2ELi64ELi3EEv5GemmP.kd
    .uniform_work_group_size: 1
    .uses_dynamic_stack: false
    .vgpr_count:     80
    .vgpr_spill_count: 0
    .wavefront_size: 64
  - .agpr_count:     16
    .args:
      - .offset:         0
        .size:           112
        .value_kind:     by_value
    .group_segment_fixed_size: 49152
    .kernarg_segment_align: 8
    .kernarg_segment_size: 112
    .language:       OpenCL C
    .language_version:
      - 2
      - 0
    .max_flat_workgroup_size: 256
    .name:           _Z6gemm_gILi64ELi64ELi32ELi32ELi0ELi3ELi64ELi3EEv5GemmP
    .private_segment_fixed_size: 0
    .sgpr_count:     30
    .sgpr_spill_count: 0
    .symbol:         _Z6gemm_gILi64ELi64ELi32ELi32ELi0ELi3ELi64ELi3EEv5GemmP.kd
    .uniform_work_group_size: 1
    .uses_dynamic_stack: false
    .vgpr_count:     56
    .vgpr_spill_count: 0
    .wavefront_size: 64
  - .agpr_count:     16
    .args:
      - .offset:         0
        .size:           112
        .value_kind:     by_value
    .group_segment_fixed_size: 49152
    .kernarg_segment_align: 8
    .kernarg_segment_size: 112
    .language:       OpenCL C
    .language_version:
      - 2
      - 0
    .max_flat_workgroup_size: 256
    .name:           _Z6gemm_gILi64ELi64ELi32ELi32ELi0ELi4ELi64ELi3EEv5GemmP
    .private_segment_fixed_size: 0
    .sgpr_count:     27
    .sgpr_spill_count: 0
    .symbol:         _Z6gemm_gILi64ELi64ELi32ELi32ELi0ELi4ELi64ELi3EEv5GemmP.kd
    .uniform_work_group_size: 1
    .uses_dynamic_stack: false
    .vgpr_count:     52
    .vgpr_spill_count: 0
    .wavefront_size: 64
  - .agpr_count:     8
    .args:
      - .offset:         0
        .size:           112
        .value_kind:     by_value
    .group_segment_fixed_size: 73728
    .kernarg_segment_align: 8
    .kernarg_segment_size: 112
    .language:       OpenCL C
    .language_version:
      - 2
      - 0
    .max_flat_workgroup_size: 256
    .name:           _Z6gemm_gILi32ELi64ELi16ELi32ELi1ELi1ELi128ELi3EEv5GemmP
    .private_segment_fixed_size: 0
    .sgpr_count:     38
    .sgpr_spill_count: 0
    .symbol:         _Z6gemm_gILi32ELi64ELi16ELi32ELi1ELi1ELi128ELi3EEv5GemmP.kd
    .uniform_work_group_size: 1
    .uses_dynamic_stack: false
    .vgpr_count:     48
    .vgpr_spill_count: 0
    .wavefront_size: 64
  - .agpr_count:     0
    .args:
      - .offset:         0
        .size:           112
        .value_kind:     by_value
    .group_segment_fixed_size: 98304
    .kernarg_segment_align: 8
    .kernarg_segment_size: 112
    .language:       OpenCL C
    .language_version:
      - 2
      - 0
    .max_flat_workgroup_size: 256
    .name:           _Z6gemm_gILi32ELi64ELi16ELi32ELi1ELi1ELi64ELi4EEv5GemmP
    .private_segment_fixed_size: 0
    .sgpr_count:     36
    .sgpr_spill_count: 0
    .symbol:         _Z6gemm_gILi32ELi64ELi16ELi32ELi1ELi1ELi64ELi4EEv5GemmP.kd
    .uniform_work_group_size: 1
    .uses_dynamic_stack: false
    .vgpr_count:     148
    .vgpr_spill_count: 0
    .wavefront_size: 64
